# v13 + grid-barrier leader tail trimmed: no XGEN add, inv overlapped with TOPGEN atomic ack
# speedup vs baseline: 1.0004x; 1.0004x over previous
.LBB0_121:
	s_or_b64 exec, exec, s[8:9]
	buffer_inv sc1
	s_waitcnt vmcnt(0)

.LBB0_342:
	s_or_b64 exec, exec, s[6:7]
	buffer_inv sc1
	s_waitcnt vmcnt(0)

.LBB0_1224:
	s_or_b64 exec, exec, s[10:11]
	buffer_inv sc1
	s_waitcnt vmcnt(0)
